# P10: next unit's schedule-table LDS reads issued inside the epilogue; the unit top reached from the epilogue only consumes them
# baseline (speedup 1.0000x reference)
.LBB0_994:
	s_lshl_b32 s4, s88, 2
	s_add_i32 s4, s4, 0
	s_add_i32 s4, s4, 0x20440
	v_mov_b32_e32 v4, v0
	v_mov_b32_e32 v2, s4
	s_nop 15
	s_nop 15
	ds_read_b32 v3, v2
	s_and_b32 s5, s90, 0x3fffff00
	v_lshlrev_b32_e32 v2, 4, v4
	s_lshl_b32 s6, s34, 8
	s_lshl_b32 s4, s90, 8
	s_lshl_b32 s5, s5, 2
	v_and_or_b32 v7, v4, 15, s25
	v_and_b32_e32 v2, 0x1ff0, v2
	s_and_b32 s4, s4, 0xff00
	s_add_i32 s7, s5, 0
	v_add_u32_e32 v5, s6, v7
	v_or_b32_e32 v2, 0x2e000000, v2
	v_and_or_b32 v4, v4, 48, s28
	s_xor_b64 s[0:1], s[92:93], -1
	s_add_i32 s7, s7, 0x20560
	v_or_b32_e32 v4, s4, v4
	v_lshl_add_u32 v6, v7, 2, s7
	s_add_i32 s98, s30, 1
	s_lshl_b32 s98, s98, 2
	s_add_i32 s98, s98, 0x21160
	v_mov_b32_e32 v233, s98
	ds_read_b32 v233, v233
	ds_read_b32 v16, v6
	ds_read_b32 v17, v6 offset:64
	ds_read_b32 v18, v6 offset:128
	ds_read_b32 v19, v6 offset:192
	ds_read_b32 v20, v6 offset:512
	ds_read_b32 v21, v6 offset:576
	ds_read_b32 v22, v6 offset:640
	ds_read_b32 v23, v6 offset:704
	s_waitcnt lgkmcnt(0)
	v_readfirstlane_b32 s98, v233
	s_max_i32 s98, s98, 0
	s_lshl_b32 s98, s98, 2
	s_add_i32 s98, s98, 0x20200
	v_mov_b32_e32 v234, s98
	ds_read_b32 v235, v234 offset:288
	ds_read_b32 v207, v234 offset:576
	ds_read_b32 v234, v234
	v_cmp_lt_i32_e32 vcc, v5, v3
	v_lshl_add_u32 v16, v16, 11, v4
	s_nop 0
	v_cndmask_b32_e32 v24, v2, v16, vcc
	v_add_u32_e32 v7, 0x10, v5
	v_cmp_lt_i32_e32 vcc, v7, v3
	v_lshl_add_u32 v17, v17, 11, v4
	s_nop 0
	v_cndmask_b32_e32 v25, v2, v17, vcc
	v_add_u32_e32 v7, 0x20, v5
	v_cmp_lt_i32_e32 vcc, v7, v3
	v_lshl_add_u32 v18, v18, 11, v4
	s_nop 0
	v_cndmask_b32_e32 v26, v2, v18, vcc
	v_add_u32_e32 v7, 0x30, v5
	v_cmp_lt_i32_e32 vcc, v7, v3
	v_lshl_add_u32 v19, v19, 11, v4
	s_nop 0
	v_cndmask_b32_e32 v27, v2, v19, vcc
	v_add_u32_e32 v7, 0x80, v5
	v_cmp_lt_i32_e32 vcc, v7, v3
	v_lshl_add_u32 v20, v20, 11, v4
	s_nop 0
	v_cndmask_b32_e32 v28, v2, v20, vcc
	v_add_u32_e32 v7, 0x90, v5
	v_cmp_lt_i32_e32 vcc, v7, v3
	v_lshl_add_u32 v21, v21, 11, v4
	s_nop 0
	v_cndmask_b32_e32 v29, v2, v21, vcc
	v_add_u32_e32 v7, 0xa0, v5
	v_cmp_lt_i32_e32 vcc, v7, v3
	v_lshl_add_u32 v22, v22, 11, v4
	s_nop 0
	v_cndmask_b32_e32 v30, v2, v22, vcc
	v_add_u32_e32 v7, 0xb0, v5
	v_cmp_lt_i32_e32 vcc, v7, v3
	v_lshl_add_u32 v23, v23, 11, v4
	s_nop 0
	v_cndmask_b32_e32 v31, v2, v23, vcc
	v_med3_f32 v32, v126, s89, v204
	v_med3_f32 v33, v127, s89, v204
	v_med3_f32 v34, v128, s89, v204
	v_med3_f32 v35, v129, s89, v204
	v_cvt_pk_fp8_f32 v8, v32, v33
	s_nop 0
	v_cvt_pk_fp8_f32 v8, v34, v35 op_sel:[0,0,1]
	v_med3_f32 v36, v130, s89, v204
	v_med3_f32 v37, v131, s89, v204
	v_med3_f32 v38, v132, s89, v204
	v_med3_f32 v39, v133, s89, v204
	v_cvt_pk_fp8_f32 v9, v36, v37
	s_nop 0
	v_cvt_pk_fp8_f32 v9, v38, v39 op_sel:[0,0,1]
	v_med3_f32 v32, v158, s89, v204
	v_med3_f32 v33, v159, s89, v204
	v_med3_f32 v34, v160, s89, v204
	v_med3_f32 v35, v161, s89, v204
	v_cvt_pk_fp8_f32 v10, v32, v33
	s_nop 0
	v_cvt_pk_fp8_f32 v10, v34, v35 op_sel:[0,0,1]
	v_med3_f32 v36, v162, s89, v204
	v_med3_f32 v37, v163, s89, v204
	v_med3_f32 v38, v164, s89, v204
	v_med3_f32 v39, v165, s89, v204
	v_cvt_pk_fp8_f32 v11, v36, v37
	s_nop 0
	v_cvt_pk_fp8_f32 v11, v38, v39 op_sel:[0,0,1]
	s_nop 0
	global_store_dwordx4 v24, v[8:11], s[78:79]
	v_med3_f32 v32, v114, s89, v204
	v_med3_f32 v33, v115, s89, v204
	v_med3_f32 v34, v116, s89, v204
	v_med3_f32 v35, v117, s89, v204
	v_cvt_pk_fp8_f32 v12, v32, v33
	s_nop 0
	v_cvt_pk_fp8_f32 v12, v34, v35 op_sel:[0,0,1]
	v_med3_f32 v36, v106, s89, v204
	v_med3_f32 v37, v107, s89, v204
	v_med3_f32 v38, v108, s89, v204
	v_med3_f32 v39, v109, s89, v204
	v_cvt_pk_fp8_f32 v13, v36, v37
	s_nop 0
	v_cvt_pk_fp8_f32 v13, v38, v39 op_sel:[0,0,1]
	v_med3_f32 v32, v154, s89, v204
	v_med3_f32 v33, v155, s89, v204
	v_med3_f32 v34, v156, s89, v204
	v_med3_f32 v35, v157, s89, v204
	v_cvt_pk_fp8_f32 v14, v32, v33
	s_nop 0
	v_cvt_pk_fp8_f32 v14, v34, v35 op_sel:[0,0,1]
	v_med3_f32 v36, v150, s89, v204
	v_med3_f32 v37, v151, s89, v204
	v_med3_f32 v38, v152, s89, v204
	v_med3_f32 v39, v153, s89, v204
	v_cvt_pk_fp8_f32 v15, v36, v37
	s_nop 0
	v_cvt_pk_fp8_f32 v15, v38, v39 op_sel:[0,0,1]
	s_nop 0
	global_store_dwordx4 v25, v[12:15], s[78:79]
	v_med3_f32 v32, v94, s89, v204
	v_med3_f32 v33, v95, s89, v204
	v_med3_f32 v34, v96, s89, v204
	v_med3_f32 v35, v97, s89, v204
	v_cvt_pk_fp8_f32 v8, v32, v33
	s_nop 0
	v_cvt_pk_fp8_f32 v8, v34, v35 op_sel:[0,0,1]
	v_med3_f32 v36, v90, s89, v204
	v_med3_f32 v37, v91, s89, v204
	v_med3_f32 v38, v92, s89, v204
	v_med3_f32 v39, v93, s89, v204
	v_cvt_pk_fp8_f32 v9, v36, v37
	s_nop 0
	v_cvt_pk_fp8_f32 v9, v38, v39 op_sel:[0,0,1]
	v_med3_f32 v32, v138, s89, v204
	v_med3_f32 v33, v139, s89, v204
	v_med3_f32 v34, v140, s89, v204
	v_med3_f32 v35, v141, s89, v204
	v_cvt_pk_fp8_f32 v10, v32, v33
	s_nop 0
	v_cvt_pk_fp8_f32 v10, v34, v35 op_sel:[0,0,1]
	v_med3_f32 v36, v134, s89, v204
	v_med3_f32 v37, v135, s89, v204
	v_med3_f32 v38, v136, s89, v204
	v_med3_f32 v39, v137, s89, v204
	v_cvt_pk_fp8_f32 v11, v36, v37
	s_nop 0
	v_cvt_pk_fp8_f32 v11, v38, v39 op_sel:[0,0,1]
	s_nop 0
	global_store_dwordx4 v26, v[8:11], s[78:79]
	v_med3_f32 v32, v78, s89, v204
	v_med3_f32 v33, v79, s89, v204
	v_med3_f32 v34, v80, s89, v204
	v_med3_f32 v35, v81, s89, v204
	v_cvt_pk_fp8_f32 v12, v32, v33
	s_nop 0
	v_cvt_pk_fp8_f32 v12, v34, v35 op_sel:[0,0,1]
	v_med3_f32 v36, v74, s89, v204
	v_med3_f32 v37, v75, s89, v204
	v_med3_f32 v38, v76, s89, v204
	v_med3_f32 v39, v77, s89, v204
	v_cvt_pk_fp8_f32 v13, v36, v37
	s_nop 0
	v_cvt_pk_fp8_f32 v13, v38, v39 op_sel:[0,0,1]
	v_med3_f32 v32, v110, s89, v204
	v_med3_f32 v33, v111, s89, v204
	v_med3_f32 v34, v112, s89, v204
	v_med3_f32 v35, v113, s89, v204
	v_cvt_pk_fp8_f32 v14, v32, v33
	s_nop 0
	v_cvt_pk_fp8_f32 v14, v34, v35 op_sel:[0,0,1]
	v_med3_f32 v36, v66, s89, v204
	v_med3_f32 v37, v67, s89, v204
	v_med3_f32 v38, v68, s89, v204
	v_med3_f32 v39, v69, s89, v204
	v_cvt_pk_fp8_f32 v15, v36, v37
	s_nop 0
	v_cvt_pk_fp8_f32 v15, v38, v39 op_sel:[0,0,1]
	s_nop 0
	global_store_dwordx4 v27, v[12:15], s[78:79]
	v_med3_f32 v32, v146, s89, v204
	v_med3_f32 v33, v147, s89, v204
	v_med3_f32 v34, v148, s89, v204
	v_med3_f32 v35, v149, s89, v204
	v_cvt_pk_fp8_f32 v8, v32, v33
	s_nop 0
	v_cvt_pk_fp8_f32 v8, v34, v35 op_sel:[0,0,1]
	v_med3_f32 v36, v142, s89, v204
	v_med3_f32 v37, v143, s89, v204
	v_med3_f32 v38, v144, s89, v204
	v_med3_f32 v39, v145, s89, v204
	v_cvt_pk_fp8_f32 v9, v36, v37
	s_nop 0
	v_cvt_pk_fp8_f32 v9, v38, v39 op_sel:[0,0,1]
	v_med3_f32 v32, v170, s89, v204
	v_med3_f32 v33, v171, s89, v204
	v_med3_f32 v34, v172, s89, v204
	v_med3_f32 v35, v173, s89, v204
	v_cvt_pk_fp8_f32 v10, v32, v33
	s_nop 0
	v_cvt_pk_fp8_f32 v10, v34, v35 op_sel:[0,0,1]
	v_med3_f32 v36, v166, s89, v204
	v_med3_f32 v37, v167, s89, v204
	v_med3_f32 v38, v168, s89, v204
	v_med3_f32 v39, v169, s89, v204
	v_cvt_pk_fp8_f32 v11, v36, v37
	s_nop 0
	v_cvt_pk_fp8_f32 v11, v38, v39 op_sel:[0,0,1]
	s_nop 0
	global_store_dwordx4 v28, v[8:11], s[78:79]
	v_med3_f32 v32, v122, s89, v204
	v_med3_f32 v33, v123, s89, v204
	v_med3_f32 v34, v124, s89, v204
	v_med3_f32 v35, v125, s89, v204
	v_cvt_pk_fp8_f32 v12, v32, v33
	s_nop 0
	v_cvt_pk_fp8_f32 v12, v34, v35 op_sel:[0,0,1]
	v_med3_f32 v36, v118, s89, v204
	v_med3_f32 v37, v119, s89, v204
	v_med3_f32 v38, v120, s89, v204
	v_med3_f32 v39, v121, s89, v204
	v_cvt_pk_fp8_f32 v13, v36, v37
	s_nop 0
	v_cvt_pk_fp8_f32 v13, v38, v39 op_sel:[0,0,1]
	v_med3_f32 v32, v62, s89, v204
	v_med3_f32 v33, v63, s89, v204
	v_med3_f32 v34, v64, s89, v204
	v_med3_f32 v35, v65, s89, v204
	v_cvt_pk_fp8_f32 v14, v32, v33
	s_nop 0
	v_cvt_pk_fp8_f32 v14, v34, v35 op_sel:[0,0,1]
	v_med3_f32 v36, v58, s89, v204
	v_med3_f32 v37, v59, s89, v204
	v_med3_f32 v38, v60, s89, v204
	v_med3_f32 v39, v61, s89, v204
	v_cvt_pk_fp8_f32 v15, v36, v37
	s_nop 0
	v_cvt_pk_fp8_f32 v15, v38, v39 op_sel:[0,0,1]
	s_nop 0
	global_store_dwordx4 v29, v[12:15], s[78:79]
	v_med3_f32 v32, v102, s89, v204
	v_med3_f32 v33, v103, s89, v204
	v_med3_f32 v34, v104, s89, v204
	v_med3_f32 v35, v105, s89, v204
	v_cvt_pk_fp8_f32 v8, v32, v33
	s_nop 0
	v_cvt_pk_fp8_f32 v8, v34, v35 op_sel:[0,0,1]
	v_med3_f32 v36, v98, s89, v204
	v_med3_f32 v37, v99, s89, v204
	v_med3_f32 v38, v100, s89, v204
	v_med3_f32 v39, v101, s89, v204
	v_cvt_pk_fp8_f32 v9, v36, v37
	s_nop 0
	v_cvt_pk_fp8_f32 v9, v38, v39 op_sel:[0,0,1]
	v_med3_f32 v32, v54, s89, v204
	v_med3_f32 v33, v55, s89, v204
	v_med3_f32 v34, v56, s89, v204
	v_med3_f32 v35, v57, s89, v204
	v_cvt_pk_fp8_f32 v10, v32, v33
	s_nop 0
	v_cvt_pk_fp8_f32 v10, v34, v35 op_sel:[0,0,1]
	v_med3_f32 v36, v50, s89, v204
	v_med3_f32 v37, v51, s89, v204
	v_med3_f32 v38, v52, s89, v204
	v_med3_f32 v39, v53, s89, v204
	v_cvt_pk_fp8_f32 v11, v36, v37
	s_nop 0
	v_cvt_pk_fp8_f32 v11, v38, v39 op_sel:[0,0,1]
	s_nop 0
	global_store_dwordx4 v30, v[8:11], s[78:79]
	v_med3_f32 v32, v86, s89, v204
	v_med3_f32 v33, v87, s89, v204
	v_med3_f32 v34, v88, s89, v204
	v_med3_f32 v35, v89, s89, v204
	v_cvt_pk_fp8_f32 v12, v32, v33
	s_nop 0
	v_cvt_pk_fp8_f32 v12, v34, v35 op_sel:[0,0,1]
	v_med3_f32 v36, v82, s89, v204
	v_med3_f32 v37, v83, s89, v204
	v_med3_f32 v38, v84, s89, v204
	v_med3_f32 v39, v85, s89, v204
	v_cvt_pk_fp8_f32 v13, v36, v37
	s_nop 0
	v_cvt_pk_fp8_f32 v13, v38, v39 op_sel:[0,0,1]
	v_med3_f32 v32, v42, s89, v204
	v_med3_f32 v33, v43, s89, v204
	v_med3_f32 v34, v44, s89, v204
	v_med3_f32 v35, v45, s89, v204
	v_cvt_pk_fp8_f32 v14, v32, v33
	s_nop 0
	v_cvt_pk_fp8_f32 v14, v34, v35 op_sel:[0,0,1]
	v_med3_f32 v36, v70, s89, v204
	v_med3_f32 v37, v71, s89, v204
	v_med3_f32 v38, v72, s89, v204
	v_med3_f32 v39, v73, s89, v204
	v_cvt_pk_fp8_f32 v15, v36, v37
	s_nop 0
	v_cvt_pk_fp8_f32 v15, v38, v39 op_sel:[0,0,1]
	s_and_b64 vcc, exec, s[0:1]
	s_mov_b32 s88, s86
	s_mov_b32 s90, s31
	s_mov_b32 s34, s91
	s_mov_b64 s[94:95], s[84:85]
	s_mov_b64 s[0:1], s[38:39]
	s_mov_b32 s16, s30
	global_store_dwordx4 v31, v[12:15], s[78:79]
	s_cbranch_vccnz .LBB0_1012
.Lp10_top2:
	s_add_i32 s30, s16, 1
	s_cmpk_gt_u32 s16, 0xfe
	s_mov_b64 s[92:93], 0
	s_cbranch_scc1 .LBB0_981
	s_waitcnt lgkmcnt(0)
	v_cmp_gt_i32_e32 vcc, 0, v233
	v_readfirstlane_b32 s4, v233
	s_cbranch_vccnz .LBB0_981
	s_mul_i32 s5, s30, s33
	s_add_i32 s6, s5, s64
	s_mov_b32 s5, s48
	v_readfirstlane_b32 s17, v234
	s_sub_i32 s6, s6, s17
	s_ashr_i32 s17, s6, 31
	s_lshr_b32 s17, s17, 29
	s_add_i32 s17, s6, s17
	s_ashr_i32 s91, s17, 3
	s_and_b32 s17, s17, -8
	s_sub_i32 s6, s6, s17
	s_mul_i32 s17, s30, 0xab
	s_bfe_u32 s17, s17, 0x70009
	s_mul_i32 s17, s17, 3
	s_sub_i32 s17, s30, s17
	s_and_b32 s17, s17, 0xff
	s_lshl_b32 s17, s17, 8
	s_or_b32 s31, s6, s17
	s_lshl_b32 s7, s91, 8
	v_readfirstlane_b32 s17, v235
	s_add_i32 s38, s7, s17
	s_ashr_i32 s39, s38, 31
	s_lshl_b64 s[38:39], s[38:39], 9
	s_add_u32 s38, s2, s38
	s_addc_u32 s39, s3, s39
	s_lshl_b64 s[50:51], s[4:5], 20
	s_add_u32 s5, s8, s50
	s_addc_u32 s17, s9, s51
	s_ashr_i32 s7, s6, 31
	s_lshl_b64 s[6:7], s[6:7], 17
	s_add_u32 s84, s5, s6
	s_addc_u32 s85, s17, s7
	s_mov_b64 s[92:93], -1
	s_mov_b32 s86, s4
	s_branch .LBB0_981
